# S5 carry scans: inputs of 32 steps loaded at once (64 dwords) instead of one global round trip per step
# speedup vs baseline: 1.0236x; 1.0020x over previous
.LBB0_1625:
	v_readlane_b32 s5, v255, 25
	s_add_i32 s14, s24, s5
	s_ashr_i32 s15, s14, 31
	s_lshl_b64 s[14:15], s[14:15], 6
	v_or_b32_e32 v2, s14, v128
	v_mov_b64_e32 v[0:1], s[58:59]
	s_movk_i32 s5, 0x88
	v_mad_u64_u32 v[0:1], s[28:29], v2, s5, v[0:1]
	v_mov_b32_e32 v2, 0x88
	v_mad_i32_i24 v1, s15, v2, v1
	v_add_co_u32_e32 v0, vcc, 0xf00000, v0
	s_waitcnt vmcnt(0)
	s_barrier
	s_nop 0
	v_addc_co_u32_e32 v1, vcc, 0, v1, vcc
	s_waitcnt vmcnt(0)
	s_waitcnt vmcnt(0)
	s_barrier
	global_load_dwordx2 v[0:1], v[0:1], off offset:128
	v_mov_b32_e32 v4, 0
	s_mov_b64 s[28:29], 0
	v_mov_b32_e32 v6, 0
	s_waitcnt vmcnt(0)
	v_pk_mov_b32 v[2:3], v[0:1], v[0:1] op_sel:[1,0]
	v_mov_b32_e32 v5, 0
.LBB0_1626:
	v_lshl_add_u64 v[8:9], v[130:131], 0, s[28:29]
	global_load_dword v16, v[8:9], off offset:-2048
	global_load_dword v17, v[8:9], off offset:-1792
	global_load_dword v18, v[8:9], off offset:-1536
	global_load_dword v19, v[8:9], off offset:-1280
	global_load_dword v20, v[8:9], off offset:-1024
	global_load_dword v21, v[8:9], off offset:-768
	global_load_dword v22, v[8:9], off offset:-512
	global_load_dword v23, v[8:9], off offset:-256
	global_load_dword v24, v[8:9], off offset:0
	global_load_dword v25, v[8:9], off offset:256
	global_load_dword v26, v[8:9], off offset:512
	global_load_dword v27, v[8:9], off offset:768
	global_load_dword v28, v[8:9], off offset:1024
	global_load_dword v29, v[8:9], off offset:1280
	global_load_dword v30, v[8:9], off offset:1536
	global_load_dword v31, v[8:9], off offset:1792
	s_add_u32 s28, s28, 0x1000
	s_addc_u32 s29, s29, 0
	v_lshl_add_u64 v[8:9], v[130:131], 0, s[28:29]
	global_load_dword v32, v[8:9], off offset:-2048
	global_load_dword v33, v[8:9], off offset:-1792
	global_load_dword v34, v[8:9], off offset:-1536
	global_load_dword v35, v[8:9], off offset:-1280
	global_load_dword v36, v[8:9], off offset:-1024
	global_load_dword v37, v[8:9], off offset:-768
	global_load_dword v38, v[8:9], off offset:-512
	global_load_dword v39, v[8:9], off offset:-256
	global_load_dword v40, v[8:9], off offset:0
	global_load_dword v41, v[8:9], off offset:256
	global_load_dword v42, v[8:9], off offset:512
	global_load_dword v43, v[8:9], off offset:768
	global_load_dword v44, v[8:9], off offset:1024
	global_load_dword v45, v[8:9], off offset:1280
	global_load_dword v46, v[8:9], off offset:1536
	global_load_dword v47, v[8:9], off offset:1792
	s_add_u32 s28, s28, 0x1000
	s_addc_u32 s29, s29, 0
	v_lshl_add_u64 v[8:9], v[130:131], 0, s[28:29]
	global_load_dword v48, v[8:9], off offset:-2048
	global_load_dword v49, v[8:9], off offset:-1792
	global_load_dword v50, v[8:9], off offset:-1536
	global_load_dword v51, v[8:9], off offset:-1280
	global_load_dword v52, v[8:9], off offset:-1024
	global_load_dword v53, v[8:9], off offset:-768
	global_load_dword v54, v[8:9], off offset:-512
	global_load_dword v55, v[8:9], off offset:-256
	global_load_dword v56, v[8:9], off offset:0
	global_load_dword v57, v[8:9], off offset:256
	global_load_dword v58, v[8:9], off offset:512
	global_load_dword v59, v[8:9], off offset:768
	global_load_dword v60, v[8:9], off offset:1024
	global_load_dword v61, v[8:9], off offset:1280
	global_load_dword v62, v[8:9], off offset:1536
	global_load_dword v63, v[8:9], off offset:1792
	s_add_u32 s28, s28, 0x1000
	s_addc_u32 s29, s29, 0
	v_lshl_add_u64 v[8:9], v[130:131], 0, s[28:29]
	global_load_dword v64, v[8:9], off offset:-2048
	global_load_dword v65, v[8:9], off offset:-1792
	global_load_dword v66, v[8:9], off offset:-1536
	global_load_dword v67, v[8:9], off offset:-1280
	global_load_dword v68, v[8:9], off offset:-1024
	global_load_dword v69, v[8:9], off offset:-768
	global_load_dword v70, v[8:9], off offset:-512
	global_load_dword v71, v[8:9], off offset:-256
	global_load_dword v72, v[8:9], off offset:0
	global_load_dword v73, v[8:9], off offset:256
	global_load_dword v74, v[8:9], off offset:512
	global_load_dword v75, v[8:9], off offset:768
	global_load_dword v76, v[8:9], off offset:1024
	global_load_dword v77, v[8:9], off offset:1280
	global_load_dword v78, v[8:9], off offset:1536
	global_load_dword v79, v[8:9], off offset:1792
	s_add_u32 s28, s28, 0x1000
	s_addc_u32 s29, s29, 0
	s_waitcnt vmcnt(0)
	v_pk_mul_f32 v[10:11], v[2:3], v[4:5] op_sel:[0,1]
	s_nop 0
	v_pk_fma_f32 v[12:13], v[0:1], v[4:5], v[10:11] neg_lo:[0,0,1] neg_hi:[0,0,1]
	v_pk_fma_f32 v[4:5], v[0:1], v[4:5], v[10:11] op_sel_hi:[1,0,1]
	s_nop 0
	v_mov_b32_e32 v13, v5
	v_pk_add_f32 v[4:5], v[12:13], v[16:17]
	s_nop 0
	v_pk_mul_f32 v[10:11], v[2:3], v[4:5] op_sel:[0,1]
	s_nop 0
	v_pk_fma_f32 v[12:13], v[0:1], v[4:5], v[10:11] neg_lo:[0,0,1] neg_hi:[0,0,1]
	v_pk_fma_f32 v[4:5], v[0:1], v[4:5], v[10:11] op_sel_hi:[1,0,1]
	s_nop 0
	v_mov_b32_e32 v13, v5
	v_pk_add_f32 v[4:5], v[12:13], v[18:19]
	s_nop 0
	v_pk_mul_f32 v[10:11], v[2:3], v[4:5] op_sel:[0,1]
	s_nop 0
	v_pk_fma_f32 v[12:13], v[0:1], v[4:5], v[10:11] neg_lo:[0,0,1] neg_hi:[0,0,1]
	v_pk_fma_f32 v[4:5], v[0:1], v[4:5], v[10:11] op_sel_hi:[1,0,1]
	s_nop 0
	v_mov_b32_e32 v13, v5
	v_pk_add_f32 v[4:5], v[12:13], v[20:21]
	s_nop 0
	v_pk_mul_f32 v[10:11], v[2:3], v[4:5] op_sel:[0,1]
	s_nop 0
	v_pk_fma_f32 v[12:13], v[0:1], v[4:5], v[10:11] neg_lo:[0,0,1] neg_hi:[0,0,1]
	v_pk_fma_f32 v[4:5], v[0:1], v[4:5], v[10:11] op_sel_hi:[1,0,1]
	s_nop 0
	v_mov_b32_e32 v13, v5
	v_pk_add_f32 v[4:5], v[12:13], v[22:23]
	s_nop 0
	v_pk_mul_f32 v[10:11], v[2:3], v[4:5] op_sel:[0,1]
	s_nop 0
	v_pk_fma_f32 v[12:13], v[0:1], v[4:5], v[10:11] neg_lo:[0,0,1] neg_hi:[0,0,1]
	v_pk_fma_f32 v[4:5], v[0:1], v[4:5], v[10:11] op_sel_hi:[1,0,1]
	s_nop 0
	v_mov_b32_e32 v13, v5
	v_pk_add_f32 v[4:5], v[12:13], v[24:25]
	s_nop 0
	v_pk_mul_f32 v[10:11], v[2:3], v[4:5] op_sel:[0,1]
	s_nop 0
	v_pk_fma_f32 v[12:13], v[0:1], v[4:5], v[10:11] neg_lo:[0,0,1] neg_hi:[0,0,1]
	v_pk_fma_f32 v[4:5], v[0:1], v[4:5], v[10:11] op_sel_hi:[1,0,1]
	s_nop 0
	v_mov_b32_e32 v13, v5
	v_pk_add_f32 v[4:5], v[12:13], v[26:27]
	s_nop 0
	v_pk_mul_f32 v[10:11], v[2:3], v[4:5] op_sel:[0,1]
	s_nop 0
	v_pk_fma_f32 v[12:13], v[0:1], v[4:5], v[10:11] neg_lo:[0,0,1] neg_hi:[0,0,1]
	v_pk_fma_f32 v[4:5], v[0:1], v[4:5], v[10:11] op_sel_hi:[1,0,1]
	s_nop 0
	v_mov_b32_e32 v13, v5
	v_pk_add_f32 v[4:5], v[12:13], v[28:29]
	s_nop 0
	v_pk_mul_f32 v[10:11], v[2:3], v[4:5] op_sel:[0,1]
	s_nop 0
	v_pk_fma_f32 v[12:13], v[0:1], v[4:5], v[10:11] neg_lo:[0,0,1] neg_hi:[0,0,1]
	v_pk_fma_f32 v[4:5], v[0:1], v[4:5], v[10:11] op_sel_hi:[1,0,1]
	s_nop 0
	v_mov_b32_e32 v13, v5
	v_pk_add_f32 v[4:5], v[12:13], v[30:31]
	s_nop 0
	v_pk_mul_f32 v[10:11], v[2:3], v[4:5] op_sel:[0,1]
	s_nop 0
	v_pk_fma_f32 v[12:13], v[0:1], v[4:5], v[10:11] neg_lo:[0,0,1] neg_hi:[0,0,1]
	v_pk_fma_f32 v[4:5], v[0:1], v[4:5], v[10:11] op_sel_hi:[1,0,1]
	s_nop 0
	v_mov_b32_e32 v13, v5
	v_pk_add_f32 v[4:5], v[12:13], v[32:33]
	s_nop 0
	v_pk_mul_f32 v[10:11], v[2:3], v[4:5] op_sel:[0,1]
	s_nop 0
	v_pk_fma_f32 v[12:13], v[0:1], v[4:5], v[10:11] neg_lo:[0,0,1] neg_hi:[0,0,1]
	v_pk_fma_f32 v[4:5], v[0:1], v[4:5], v[10:11] op_sel_hi:[1,0,1]
	s_nop 0
	v_mov_b32_e32 v13, v5
	v_pk_add_f32 v[4:5], v[12:13], v[34:35]
	s_nop 0
	v_pk_mul_f32 v[10:11], v[2:3], v[4:5] op_sel:[0,1]
	s_nop 0
	v_pk_fma_f32 v[12:13], v[0:1], v[4:5], v[10:11] neg_lo:[0,0,1] neg_hi:[0,0,1]
	v_pk_fma_f32 v[4:5], v[0:1], v[4:5], v[10:11] op_sel_hi:[1,0,1]
	s_nop 0
	v_mov_b32_e32 v13, v5
	v_pk_add_f32 v[4:5], v[12:13], v[36:37]
	s_nop 0
	v_pk_mul_f32 v[10:11], v[2:3], v[4:5] op_sel:[0,1]
	s_nop 0
	v_pk_fma_f32 v[12:13], v[0:1], v[4:5], v[10:11] neg_lo:[0,0,1] neg_hi:[0,0,1]
	v_pk_fma_f32 v[4:5], v[0:1], v[4:5], v[10:11] op_sel_hi:[1,0,1]
	s_nop 0
	v_mov_b32_e32 v13, v5
	v_pk_add_f32 v[4:5], v[12:13], v[38:39]
	s_nop 0
	v_pk_mul_f32 v[10:11], v[2:3], v[4:5] op_sel:[0,1]
	s_nop 0
	v_pk_fma_f32 v[12:13], v[0:1], v[4:5], v[10:11] neg_lo:[0,0,1] neg_hi:[0,0,1]
	v_pk_fma_f32 v[4:5], v[0:1], v[4:5], v[10:11] op_sel_hi:[1,0,1]
	s_nop 0
	v_mov_b32_e32 v13, v5
	v_pk_add_f32 v[4:5], v[12:13], v[40:41]
	s_nop 0
	v_pk_mul_f32 v[10:11], v[2:3], v[4:5] op_sel:[0,1]
	s_nop 0
	v_pk_fma_f32 v[12:13], v[0:1], v[4:5], v[10:11] neg_lo:[0,0,1] neg_hi:[0,0,1]
	v_pk_fma_f32 v[4:5], v[0:1], v[4:5], v[10:11] op_sel_hi:[1,0,1]
	s_nop 0
	v_mov_b32_e32 v13, v5
	v_pk_add_f32 v[4:5], v[12:13], v[42:43]
	s_nop 0
	v_pk_mul_f32 v[10:11], v[2:3], v[4:5] op_sel:[0,1]
	s_nop 0
	v_pk_fma_f32 v[12:13], v[0:1], v[4:5], v[10:11] neg_lo:[0,0,1] neg_hi:[0,0,1]
	v_pk_fma_f32 v[4:5], v[0:1], v[4:5], v[10:11] op_sel_hi:[1,0,1]
	s_nop 0
	v_mov_b32_e32 v13, v5
	v_pk_add_f32 v[4:5], v[12:13], v[44:45]
	s_nop 0
	v_pk_mul_f32 v[10:11], v[2:3], v[4:5] op_sel:[0,1]
	s_nop 0
	v_pk_fma_f32 v[12:13], v[0:1], v[4:5], v[10:11] neg_lo:[0,0,1] neg_hi:[0,0,1]
	v_pk_fma_f32 v[4:5], v[0:1], v[4:5], v[10:11] op_sel_hi:[1,0,1]
	s_nop 0
	v_mov_b32_e32 v13, v5
	v_pk_add_f32 v[4:5], v[12:13], v[46:47]
	s_nop 0
	v_pk_mul_f32 v[10:11], v[2:3], v[4:5] op_sel:[0,1]
	s_nop 0
	v_pk_fma_f32 v[12:13], v[0:1], v[4:5], v[10:11] neg_lo:[0,0,1] neg_hi:[0,0,1]
	v_pk_fma_f32 v[4:5], v[0:1], v[4:5], v[10:11] op_sel_hi:[1,0,1]
	s_nop 0
	v_mov_b32_e32 v13, v5
	v_pk_add_f32 v[4:5], v[12:13], v[48:49]
	s_nop 0
	v_pk_mul_f32 v[10:11], v[2:3], v[4:5] op_sel:[0,1]
	s_nop 0
	v_pk_fma_f32 v[12:13], v[0:1], v[4:5], v[10:11] neg_lo:[0,0,1] neg_hi:[0,0,1]
	v_pk_fma_f32 v[4:5], v[0:1], v[4:5], v[10:11] op_sel_hi:[1,0,1]
	s_nop 0
	v_mov_b32_e32 v13, v5
	v_pk_add_f32 v[4:5], v[12:13], v[50:51]
	s_nop 0
	v_pk_mul_f32 v[10:11], v[2:3], v[4:5] op_sel:[0,1]
	s_nop 0
	v_pk_fma_f32 v[12:13], v[0:1], v[4:5], v[10:11] neg_lo:[0,0,1] neg_hi:[0,0,1]
	v_pk_fma_f32 v[4:5], v[0:1], v[4:5], v[10:11] op_sel_hi:[1,0,1]
	s_nop 0
	v_mov_b32_e32 v13, v5
	v_pk_add_f32 v[4:5], v[12:13], v[52:53]
	s_nop 0
	v_pk_mul_f32 v[10:11], v[2:3], v[4:5] op_sel:[0,1]
	s_nop 0
	v_pk_fma_f32 v[12:13], v[0:1], v[4:5], v[10:11] neg_lo:[0,0,1] neg_hi:[0,0,1]
	v_pk_fma_f32 v[4:5], v[0:1], v[4:5], v[10:11] op_sel_hi:[1,0,1]
	s_nop 0
	v_mov_b32_e32 v13, v5
	v_pk_add_f32 v[4:5], v[12:13], v[54:55]
	s_nop 0
	v_pk_mul_f32 v[10:11], v[2:3], v[4:5] op_sel:[0,1]
	s_nop 0
	v_pk_fma_f32 v[12:13], v[0:1], v[4:5], v[10:11] neg_lo:[0,0,1] neg_hi:[0,0,1]
	v_pk_fma_f32 v[4:5], v[0:1], v[4:5], v[10:11] op_sel_hi:[1,0,1]
	s_nop 0
	v_mov_b32_e32 v13, v5
	v_pk_add_f32 v[4:5], v[12:13], v[56:57]
	s_nop 0
	v_pk_mul_f32 v[10:11], v[2:3], v[4:5] op_sel:[0,1]
	s_nop 0
	v_pk_fma_f32 v[12:13], v[0:1], v[4:5], v[10:11] neg_lo:[0,0,1] neg_hi:[0,0,1]
	v_pk_fma_f32 v[4:5], v[0:1], v[4:5], v[10:11] op_sel_hi:[1,0,1]
	s_nop 0
	v_mov_b32_e32 v13, v5
	v_pk_add_f32 v[4:5], v[12:13], v[58:59]
	s_nop 0
	v_pk_mul_f32 v[10:11], v[2:3], v[4:5] op_sel:[0,1]
	s_nop 0
	v_pk_fma_f32 v[12:13], v[0:1], v[4:5], v[10:11] neg_lo:[0,0,1] neg_hi:[0,0,1]
	v_pk_fma_f32 v[4:5], v[0:1], v[4:5], v[10:11] op_sel_hi:[1,0,1]
	s_nop 0
	v_mov_b32_e32 v13, v5
	v_pk_add_f32 v[4:5], v[12:13], v[60:61]
	s_nop 0
	v_pk_mul_f32 v[10:11], v[2:3], v[4:5] op_sel:[0,1]
	s_nop 0
	v_pk_fma_f32 v[12:13], v[0:1], v[4:5], v[10:11] neg_lo:[0,0,1] neg_hi:[0,0,1]
	v_pk_fma_f32 v[4:5], v[0:1], v[4:5], v[10:11] op_sel_hi:[1,0,1]
	s_nop 0
	v_mov_b32_e32 v13, v5
	v_pk_add_f32 v[4:5], v[12:13], v[62:63]
	s_nop 0
	v_pk_mul_f32 v[10:11], v[2:3], v[4:5] op_sel:[0,1]
	s_nop 0
	v_pk_fma_f32 v[12:13], v[0:1], v[4:5], v[10:11] neg_lo:[0,0,1] neg_hi:[0,0,1]
	v_pk_fma_f32 v[4:5], v[0:1], v[4:5], v[10:11] op_sel_hi:[1,0,1]
	s_nop 0
	v_mov_b32_e32 v13, v5
	v_pk_add_f32 v[4:5], v[12:13], v[64:65]
	s_nop 0
	v_pk_mul_f32 v[10:11], v[2:3], v[4:5] op_sel:[0,1]
	s_nop 0
	v_pk_fma_f32 v[12:13], v[0:1], v[4:5], v[10:11] neg_lo:[0,0,1] neg_hi:[0,0,1]
	v_pk_fma_f32 v[4:5], v[0:1], v[4:5], v[10:11] op_sel_hi:[1,0,1]
	s_nop 0
	v_mov_b32_e32 v13, v5
	v_pk_add_f32 v[4:5], v[12:13], v[66:67]
	s_nop 0
	v_pk_mul_f32 v[10:11], v[2:3], v[4:5] op_sel:[0,1]
	s_nop 0
	v_pk_fma_f32 v[12:13], v[0:1], v[4:5], v[10:11] neg_lo:[0,0,1] neg_hi:[0,0,1]
	v_pk_fma_f32 v[4:5], v[0:1], v[4:5], v[10:11] op_sel_hi:[1,0,1]
	s_nop 0
	v_mov_b32_e32 v13, v5
	v_pk_add_f32 v[4:5], v[12:13], v[68:69]
	s_nop 0
	v_pk_mul_f32 v[10:11], v[2:3], v[4:5] op_sel:[0,1]
	s_nop 0
	v_pk_fma_f32 v[12:13], v[0:1], v[4:5], v[10:11] neg_lo:[0,0,1] neg_hi:[0,0,1]
	v_pk_fma_f32 v[4:5], v[0:1], v[4:5], v[10:11] op_sel_hi:[1,0,1]
	s_nop 0
	v_mov_b32_e32 v13, v5
	v_pk_add_f32 v[4:5], v[12:13], v[70:71]
	s_nop 0
	v_pk_mul_f32 v[10:11], v[2:3], v[4:5] op_sel:[0,1]
	s_nop 0
	v_pk_fma_f32 v[12:13], v[0:1], v[4:5], v[10:11] neg_lo:[0,0,1] neg_hi:[0,0,1]
	v_pk_fma_f32 v[4:5], v[0:1], v[4:5], v[10:11] op_sel_hi:[1,0,1]
	s_nop 0
	v_mov_b32_e32 v13, v5
	v_pk_add_f32 v[4:5], v[12:13], v[72:73]
	s_nop 0
	v_pk_mul_f32 v[10:11], v[2:3], v[4:5] op_sel:[0,1]
	s_nop 0
	v_pk_fma_f32 v[12:13], v[0:1], v[4:5], v[10:11] neg_lo:[0,0,1] neg_hi:[0,0,1]
	v_pk_fma_f32 v[4:5], v[0:1], v[4:5], v[10:11] op_sel_hi:[1,0,1]
	s_nop 0
	v_mov_b32_e32 v13, v5
	v_pk_add_f32 v[4:5], v[12:13], v[74:75]
	s_nop 0
	v_pk_mul_f32 v[10:11], v[2:3], v[4:5] op_sel:[0,1]
	s_nop 0
	v_pk_fma_f32 v[12:13], v[0:1], v[4:5], v[10:11] neg_lo:[0,0,1] neg_hi:[0,0,1]
	v_pk_fma_f32 v[4:5], v[0:1], v[4:5], v[10:11] op_sel_hi:[1,0,1]
	s_nop 0
	v_mov_b32_e32 v13, v5
	v_pk_add_f32 v[4:5], v[12:13], v[76:77]
	s_nop 0
	v_pk_mul_f32 v[10:11], v[2:3], v[4:5] op_sel:[0,1]
	s_nop 0
	v_pk_fma_f32 v[12:13], v[0:1], v[4:5], v[10:11] neg_lo:[0,0,1] neg_hi:[0,0,1]
	v_pk_fma_f32 v[4:5], v[0:1], v[4:5], v[10:11] op_sel_hi:[1,0,1]
	s_nop 0
	v_mov_b32_e32 v13, v5
	v_pk_add_f32 v[4:5], v[12:13], v[78:79]
	s_nop 0
	v_mov_b32_e32 v6, v5
	s_cmp_eq_u32 s28, 0x10000
	s_cbranch_scc0 .LBB0_1626
	v_mov_b32_e32 v176, v177
	v_mov_b64_e32 v[6:7], v[176:177]
	s_barrier
	ds_write_b64 v149, v[4:5]
	s_waitcnt lgkmcnt(0)
	s_barrier
	s_and_saveexec_b64 s[28:29], s[38:39]
	s_movk_i32 s70, 0x300
	s_cbranch_execz .LBB0_1631
	v_pk_mul_f32 v[4:5], v[0:1], v[0:1]
	s_mov_b64 s[14:15], 0
	v_sub_f32_e32 v4, v4, v5
	v_add_f32_e32 v5, v0, v0
	v_mul_f32_e32 v5, v1, v5
	v_mul_f32_e32 v6, v4, v4
	v_add_f32_e32 v4, v4, v4
	v_mul_f32_e32 v4, v5, v4
	v_fma_f32 v6, -v5, v5, v6
	v_mul_f32_e32 v5, v4, v4
	v_fma_f32 v5, v6, v6, -v5
	v_add_f32_e32 v6, v6, v6
	v_mul_f32_e32 v4, v4, v6
	v_mul_f32_e32 v6, v4, v4
	v_fma_f32 v6, v5, v5, -v6
	v_add_f32_e32 v5, v5, v5
	v_mul_f32_e32 v4, v4, v5
	v_mul_f32_e32 v5, v4, v4
	v_fma_f32 v5, v6, v6, -v5
	v_add_f32_e32 v6, v6, v6
	v_mul_f32_e32 v4, v4, v6
	v_mul_f32_e32 v6, v4, v4
	v_fma_f32 v6, v5, v5, -v6
	v_add_f32_e32 v5, v5, v5
	v_mul_f32_e32 v5, v4, v5
	v_mul_f32_e32 v4, v5, v5
	v_fma_f32 v4, v6, v6, -v4
	v_add_f32_e32 v6, v6, v6
	v_mul_f32_e32 v8, v5, v6
	v_mov_b32_e32 v6, 0
	v_mov_b32_e32 v5, v4
	v_mov_b32_e32 v9, v8
	v_mov_b32_e32 v10, v148
	v_mov_b32_e32 v11, v129
	v_mov_b32_e32 v7, v6

.LBB0_1632:
	v_lshl_add_u64 v[8:9], v[134:135], 0, s[28:29]
	global_load_dword v16, v[8:9], off offset:-1024
	global_load_dword v17, v[8:9], off offset:-768
	global_load_dword v18, v[8:9], off offset:-512
	global_load_dword v19, v[8:9], off offset:-256
	global_load_dword v20, v[8:9], off offset:0
	global_load_dword v21, v[8:9], off offset:256
	global_load_dword v22, v[8:9], off offset:512
	global_load_dword v23, v[8:9], off offset:768
	s_add_u32 s28, s28, 0x800
	s_addc_u32 s29, s29, 0
	v_lshl_add_u64 v[8:9], v[134:135], 0, s[28:29]
	global_load_dword v24, v[8:9], off offset:-1024
	global_load_dword v25, v[8:9], off offset:-768
	global_load_dword v26, v[8:9], off offset:-512
	global_load_dword v27, v[8:9], off offset:-256
	global_load_dword v28, v[8:9], off offset:0
	global_load_dword v29, v[8:9], off offset:256
	global_load_dword v30, v[8:9], off offset:512
	global_load_dword v31, v[8:9], off offset:768
	s_add_u32 s28, s28, 0x800
	s_addc_u32 s29, s29, 0
	v_lshl_add_u64 v[8:9], v[134:135], 0, s[28:29]
	global_load_dword v32, v[8:9], off offset:-1024
	global_load_dword v33, v[8:9], off offset:-768
	global_load_dword v34, v[8:9], off offset:-512
	global_load_dword v35, v[8:9], off offset:-256
	global_load_dword v36, v[8:9], off offset:0
	global_load_dword v37, v[8:9], off offset:256
	global_load_dword v38, v[8:9], off offset:512
	global_load_dword v39, v[8:9], off offset:768
	s_add_u32 s28, s28, 0x800
	s_addc_u32 s29, s29, 0
	v_lshl_add_u64 v[8:9], v[134:135], 0, s[28:29]
	global_load_dword v40, v[8:9], off offset:-1024
	global_load_dword v41, v[8:9], off offset:-768
	global_load_dword v42, v[8:9], off offset:-512
	global_load_dword v43, v[8:9], off offset:-256
	global_load_dword v44, v[8:9], off offset:0
	global_load_dword v45, v[8:9], off offset:256
	global_load_dword v46, v[8:9], off offset:512
	global_load_dword v47, v[8:9], off offset:768
	s_add_u32 s28, s28, 0x800
	s_addc_u32 s29, s29, 0
	v_lshl_add_u64 v[8:9], v[134:135], 0, s[28:29]
	global_load_dword v48, v[8:9], off offset:-1024
	global_load_dword v49, v[8:9], off offset:-768
	global_load_dword v50, v[8:9], off offset:-512
	global_load_dword v51, v[8:9], off offset:-256
	global_load_dword v52, v[8:9], off offset:0
	global_load_dword v53, v[8:9], off offset:256
	global_load_dword v54, v[8:9], off offset:512
	global_load_dword v55, v[8:9], off offset:768
	s_add_u32 s28, s28, 0x800
	s_addc_u32 s29, s29, 0
	v_lshl_add_u64 v[8:9], v[134:135], 0, s[28:29]
	global_load_dword v56, v[8:9], off offset:-1024
	global_load_dword v57, v[8:9], off offset:-768
	global_load_dword v58, v[8:9], off offset:-512
	global_load_dword v59, v[8:9], off offset:-256
	global_load_dword v60, v[8:9], off offset:0
	global_load_dword v61, v[8:9], off offset:256
	global_load_dword v62, v[8:9], off offset:512
	global_load_dword v63, v[8:9], off offset:768
	s_add_u32 s28, s28, 0x800
	s_addc_u32 s29, s29, 0
	v_lshl_add_u64 v[8:9], v[134:135], 0, s[28:29]
	global_load_dword v64, v[8:9], off offset:-1024
	global_load_dword v65, v[8:9], off offset:-768
	global_load_dword v66, v[8:9], off offset:-512
	global_load_dword v67, v[8:9], off offset:-256
	global_load_dword v68, v[8:9], off offset:0
	global_load_dword v69, v[8:9], off offset:256
	global_load_dword v70, v[8:9], off offset:512
	global_load_dword v71, v[8:9], off offset:768
	s_add_u32 s28, s28, 0x800
	s_addc_u32 s29, s29, 0
	v_lshl_add_u64 v[8:9], v[134:135], 0, s[28:29]
	global_load_dword v72, v[8:9], off offset:-1024
	global_load_dword v73, v[8:9], off offset:-768
	global_load_dword v74, v[8:9], off offset:-512
	global_load_dword v75, v[8:9], off offset:-256
	global_load_dword v76, v[8:9], off offset:0
	global_load_dword v77, v[8:9], off offset:256
	global_load_dword v78, v[8:9], off offset:512
	global_load_dword v79, v[8:9], off offset:768
	s_add_u32 s28, s28, 0x800
	s_addc_u32 s29, s29, 0
	s_mov_b64 s[14:15], 0xc00
	s_waitcnt vmcnt(0)
	v_cvt_pk_bf16_f32 v14, v6, v177
	v_cvt_pk_bf16_f32 v15, v7, v177
	global_store_short v[4:5], v14, off offset:-1536
	global_store_short v[4:5], v15, off offset:-1408
	v_pk_mul_f32 v[10:11], v[2:3], v[6:7] op_sel:[0,1]
	s_nop 0
	v_pk_fma_f32 v[12:13], v[0:1], v[6:7], v[10:11] neg_lo:[0,0,1] neg_hi:[0,0,1]
	v_pk_fma_f32 v[6:7], v[0:1], v[6:7], v[10:11] op_sel_hi:[1,0,1]
	s_nop 0
	v_mov_b32_e32 v13, v7
	v_pk_add_f32 v[6:7], v[12:13], v[16:17]
	s_nop 0
	v_cvt_pk_bf16_f32 v14, v6, v177
	v_cvt_pk_bf16_f32 v15, v7, v177
	global_store_short v[4:5], v14, off offset:-768
	global_store_short v[4:5], v15, off offset:-640
	v_pk_mul_f32 v[10:11], v[2:3], v[6:7] op_sel:[0,1]
	s_nop 0
	v_pk_fma_f32 v[12:13], v[0:1], v[6:7], v[10:11] neg_lo:[0,0,1] neg_hi:[0,0,1]
	v_pk_fma_f32 v[6:7], v[0:1], v[6:7], v[10:11] op_sel_hi:[1,0,1]
	s_nop 0
	v_mov_b32_e32 v13, v7
	v_pk_add_f32 v[6:7], v[12:13], v[18:19]
	s_nop 0
	v_cvt_pk_bf16_f32 v14, v6, v177
	v_cvt_pk_bf16_f32 v15, v7, v177
	global_store_short v[4:5], v14, off
	global_store_short v[4:5], v15, off offset:128
	v_pk_mul_f32 v[10:11], v[2:3], v[6:7] op_sel:[0,1]
	s_nop 0
	v_pk_fma_f32 v[12:13], v[0:1], v[6:7], v[10:11] neg_lo:[0,0,1] neg_hi:[0,0,1]
	v_pk_fma_f32 v[6:7], v[0:1], v[6:7], v[10:11] op_sel_hi:[1,0,1]
	s_nop 0
	v_mov_b32_e32 v13, v7
	v_pk_add_f32 v[6:7], v[12:13], v[20:21]
	s_nop 0
	v_cvt_pk_bf16_f32 v14, v6, v177
	v_cvt_pk_bf16_f32 v15, v7, v177
	global_store_short v[4:5], v14, off offset:768
	global_store_short v[4:5], v15, off offset:896
	v_pk_mul_f32 v[10:11], v[2:3], v[6:7] op_sel:[0,1]
	s_nop 0
	v_pk_fma_f32 v[12:13], v[0:1], v[6:7], v[10:11] neg_lo:[0,0,1] neg_hi:[0,0,1]
	v_pk_fma_f32 v[6:7], v[0:1], v[6:7], v[10:11] op_sel_hi:[1,0,1]
	s_nop 0
	v_mov_b32_e32 v13, v7
	v_pk_add_f32 v[6:7], v[12:13], v[22:23]
	s_nop 0
	v_lshl_add_u64 v[4:5], v[4:5], 0, s[14:15]
	v_cvt_pk_bf16_f32 v14, v6, v177
	v_cvt_pk_bf16_f32 v15, v7, v177
	global_store_short v[4:5], v14, off offset:-1536
	global_store_short v[4:5], v15, off offset:-1408
	v_pk_mul_f32 v[10:11], v[2:3], v[6:7] op_sel:[0,1]
	s_nop 0
	v_pk_fma_f32 v[12:13], v[0:1], v[6:7], v[10:11] neg_lo:[0,0,1] neg_hi:[0,0,1]
	v_pk_fma_f32 v[6:7], v[0:1], v[6:7], v[10:11] op_sel_hi:[1,0,1]
	s_nop 0
	v_mov_b32_e32 v13, v7
	v_pk_add_f32 v[6:7], v[12:13], v[24:25]
	s_nop 0
	v_cvt_pk_bf16_f32 v14, v6, v177
	v_cvt_pk_bf16_f32 v15, v7, v177
	global_store_short v[4:5], v14, off offset:-768
	global_store_short v[4:5], v15, off offset:-640
	v_pk_mul_f32 v[10:11], v[2:3], v[6:7] op_sel:[0,1]
	s_nop 0
	v_pk_fma_f32 v[12:13], v[0:1], v[6:7], v[10:11] neg_lo:[0,0,1] neg_hi:[0,0,1]
	v_pk_fma_f32 v[6:7], v[0:1], v[6:7], v[10:11] op_sel_hi:[1,0,1]
	s_nop 0
	v_mov_b32_e32 v13, v7
	v_pk_add_f32 v[6:7], v[12:13], v[26:27]
	s_nop 0
	v_cvt_pk_bf16_f32 v14, v6, v177
	v_cvt_pk_bf16_f32 v15, v7, v177
	global_store_short v[4:5], v14, off
	global_store_short v[4:5], v15, off offset:128
	v_pk_mul_f32 v[10:11], v[2:3], v[6:7] op_sel:[0,1]
	s_nop 0
	v_pk_fma_f32 v[12:13], v[0:1], v[6:7], v[10:11] neg_lo:[0,0,1] neg_hi:[0,0,1]
	v_pk_fma_f32 v[6:7], v[0:1], v[6:7], v[10:11] op_sel_hi:[1,0,1]
	s_nop 0
	v_mov_b32_e32 v13, v7
	v_pk_add_f32 v[6:7], v[12:13], v[28:29]
	s_nop 0
	v_cvt_pk_bf16_f32 v14, v6, v177
	v_cvt_pk_bf16_f32 v15, v7, v177
	global_store_short v[4:5], v14, off offset:768
	global_store_short v[4:5], v15, off offset:896
	v_pk_mul_f32 v[10:11], v[2:3], v[6:7] op_sel:[0,1]
	s_nop 0
	v_pk_fma_f32 v[12:13], v[0:1], v[6:7], v[10:11] neg_lo:[0,0,1] neg_hi:[0,0,1]
	v_pk_fma_f32 v[6:7], v[0:1], v[6:7], v[10:11] op_sel_hi:[1,0,1]
	s_nop 0
	v_mov_b32_e32 v13, v7
	v_pk_add_f32 v[6:7], v[12:13], v[30:31]
	s_nop 0
	v_lshl_add_u64 v[4:5], v[4:5], 0, s[14:15]
	v_cvt_pk_bf16_f32 v14, v6, v177
	v_cvt_pk_bf16_f32 v15, v7, v177
	global_store_short v[4:5], v14, off offset:-1536
	global_store_short v[4:5], v15, off offset:-1408
	v_pk_mul_f32 v[10:11], v[2:3], v[6:7] op_sel:[0,1]
	s_nop 0
	v_pk_fma_f32 v[12:13], v[0:1], v[6:7], v[10:11] neg_lo:[0,0,1] neg_hi:[0,0,1]
	v_pk_fma_f32 v[6:7], v[0:1], v[6:7], v[10:11] op_sel_hi:[1,0,1]
	s_nop 0
	v_mov_b32_e32 v13, v7
	v_pk_add_f32 v[6:7], v[12:13], v[32:33]
	s_nop 0
	v_cvt_pk_bf16_f32 v14, v6, v177
	v_cvt_pk_bf16_f32 v15, v7, v177
	global_store_short v[4:5], v14, off offset:-768
	global_store_short v[4:5], v15, off offset:-640
	v_pk_mul_f32 v[10:11], v[2:3], v[6:7] op_sel:[0,1]
	s_nop 0
	v_pk_fma_f32 v[12:13], v[0:1], v[6:7], v[10:11] neg_lo:[0,0,1] neg_hi:[0,0,1]
	v_pk_fma_f32 v[6:7], v[0:1], v[6:7], v[10:11] op_sel_hi:[1,0,1]
	s_nop 0
	v_mov_b32_e32 v13, v7
	v_pk_add_f32 v[6:7], v[12:13], v[34:35]
	s_nop 0
	v_cvt_pk_bf16_f32 v14, v6, v177
	v_cvt_pk_bf16_f32 v15, v7, v177
	global_store_short v[4:5], v14, off
	global_store_short v[4:5], v15, off offset:128
	v_pk_mul_f32 v[10:11], v[2:3], v[6:7] op_sel:[0,1]
	s_nop 0
	v_pk_fma_f32 v[12:13], v[0:1], v[6:7], v[10:11] neg_lo:[0,0,1] neg_hi:[0,0,1]
	v_pk_fma_f32 v[6:7], v[0:1], v[6:7], v[10:11] op_sel_hi:[1,0,1]
	s_nop 0
	v_mov_b32_e32 v13, v7
	v_pk_add_f32 v[6:7], v[12:13], v[36:37]
	s_nop 0
	v_cvt_pk_bf16_f32 v14, v6, v177
	v_cvt_pk_bf16_f32 v15, v7, v177
	global_store_short v[4:5], v14, off offset:768
	global_store_short v[4:5], v15, off offset:896
	v_pk_mul_f32 v[10:11], v[2:3], v[6:7] op_sel:[0,1]
	s_nop 0
	v_pk_fma_f32 v[12:13], v[0:1], v[6:7], v[10:11] neg_lo:[0,0,1] neg_hi:[0,0,1]
	v_pk_fma_f32 v[6:7], v[0:1], v[6:7], v[10:11] op_sel_hi:[1,0,1]
	s_nop 0
	v_mov_b32_e32 v13, v7
	v_pk_add_f32 v[6:7], v[12:13], v[38:39]
	s_nop 0
	v_lshl_add_u64 v[4:5], v[4:5], 0, s[14:15]
	v_cvt_pk_bf16_f32 v14, v6, v177
	v_cvt_pk_bf16_f32 v15, v7, v177
	global_store_short v[4:5], v14, off offset:-1536
	global_store_short v[4:5], v15, off offset:-1408
	v_pk_mul_f32 v[10:11], v[2:3], v[6:7] op_sel:[0,1]
	s_nop 0
	v_pk_fma_f32 v[12:13], v[0:1], v[6:7], v[10:11] neg_lo:[0,0,1] neg_hi:[0,0,1]
	v_pk_fma_f32 v[6:7], v[0:1], v[6:7], v[10:11] op_sel_hi:[1,0,1]
	s_nop 0
	v_mov_b32_e32 v13, v7
	v_pk_add_f32 v[6:7], v[12:13], v[40:41]
	s_nop 0
	v_cvt_pk_bf16_f32 v14, v6, v177
	v_cvt_pk_bf16_f32 v15, v7, v177
	global_store_short v[4:5], v14, off offset:-768
	global_store_short v[4:5], v15, off offset:-640
	v_pk_mul_f32 v[10:11], v[2:3], v[6:7] op_sel:[0,1]
	s_nop 0
	v_pk_fma_f32 v[12:13], v[0:1], v[6:7], v[10:11] neg_lo:[0,0,1] neg_hi:[0,0,1]
	v_pk_fma_f32 v[6:7], v[0:1], v[6:7], v[10:11] op_sel_hi:[1,0,1]
	s_nop 0
	v_mov_b32_e32 v13, v7
	v_pk_add_f32 v[6:7], v[12:13], v[42:43]
	s_nop 0
	v_cvt_pk_bf16_f32 v14, v6, v177
	v_cvt_pk_bf16_f32 v15, v7, v177
	global_store_short v[4:5], v14, off
	global_store_short v[4:5], v15, off offset:128
	v_pk_mul_f32 v[10:11], v[2:3], v[6:7] op_sel:[0,1]
	s_nop 0
	v_pk_fma_f32 v[12:13], v[0:1], v[6:7], v[10:11] neg_lo:[0,0,1] neg_hi:[0,0,1]
	v_pk_fma_f32 v[6:7], v[0:1], v[6:7], v[10:11] op_sel_hi:[1,0,1]
	s_nop 0
	v_mov_b32_e32 v13, v7
	v_pk_add_f32 v[6:7], v[12:13], v[44:45]
	s_nop 0
	v_cvt_pk_bf16_f32 v14, v6, v177
	v_cvt_pk_bf16_f32 v15, v7, v177
	global_store_short v[4:5], v14, off offset:768
	global_store_short v[4:5], v15, off offset:896
	v_pk_mul_f32 v[10:11], v[2:3], v[6:7] op_sel:[0,1]
	s_nop 0
	v_pk_fma_f32 v[12:13], v[0:1], v[6:7], v[10:11] neg_lo:[0,0,1] neg_hi:[0,0,1]
	v_pk_fma_f32 v[6:7], v[0:1], v[6:7], v[10:11] op_sel_hi:[1,0,1]
	s_nop 0
	v_mov_b32_e32 v13, v7
	v_pk_add_f32 v[6:7], v[12:13], v[46:47]
	s_nop 0
	v_lshl_add_u64 v[4:5], v[4:5], 0, s[14:15]
	v_cvt_pk_bf16_f32 v14, v6, v177
	v_cvt_pk_bf16_f32 v15, v7, v177
	global_store_short v[4:5], v14, off offset:-1536
	global_store_short v[4:5], v15, off offset:-1408
	v_pk_mul_f32 v[10:11], v[2:3], v[6:7] op_sel:[0,1]
	s_nop 0
	v_pk_fma_f32 v[12:13], v[0:1], v[6:7], v[10:11] neg_lo:[0,0,1] neg_hi:[0,0,1]
	v_pk_fma_f32 v[6:7], v[0:1], v[6:7], v[10:11] op_sel_hi:[1,0,1]
	s_nop 0
	v_mov_b32_e32 v13, v7
	v_pk_add_f32 v[6:7], v[12:13], v[48:49]
	s_nop 0
	v_cvt_pk_bf16_f32 v14, v6, v177
	v_cvt_pk_bf16_f32 v15, v7, v177
	global_store_short v[4:5], v14, off offset:-768
	global_store_short v[4:5], v15, off offset:-640
	v_pk_mul_f32 v[10:11], v[2:3], v[6:7] op_sel:[0,1]
	s_nop 0
	v_pk_fma_f32 v[12:13], v[0:1], v[6:7], v[10:11] neg_lo:[0,0,1] neg_hi:[0,0,1]
	v_pk_fma_f32 v[6:7], v[0:1], v[6:7], v[10:11] op_sel_hi:[1,0,1]
	s_nop 0
	v_mov_b32_e32 v13, v7
	v_pk_add_f32 v[6:7], v[12:13], v[50:51]
	s_nop 0
	v_cvt_pk_bf16_f32 v14, v6, v177
	v_cvt_pk_bf16_f32 v15, v7, v177
	global_store_short v[4:5], v14, off
	global_store_short v[4:5], v15, off offset:128
	v_pk_mul_f32 v[10:11], v[2:3], v[6:7] op_sel:[0,1]
	s_nop 0
	v_pk_fma_f32 v[12:13], v[0:1], v[6:7], v[10:11] neg_lo:[0,0,1] neg_hi:[0,0,1]
	v_pk_fma_f32 v[6:7], v[0:1], v[6:7], v[10:11] op_sel_hi:[1,0,1]
	s_nop 0
	v_mov_b32_e32 v13, v7
	v_pk_add_f32 v[6:7], v[12:13], v[52:53]
	s_nop 0
	v_cvt_pk_bf16_f32 v14, v6, v177
	v_cvt_pk_bf16_f32 v15, v7, v177
	global_store_short v[4:5], v14, off offset:768
	global_store_short v[4:5], v15, off offset:896
	v_pk_mul_f32 v[10:11], v[2:3], v[6:7] op_sel:[0,1]
	s_nop 0
	v_pk_fma_f32 v[12:13], v[0:1], v[6:7], v[10:11] neg_lo:[0,0,1] neg_hi:[0,0,1]
	v_pk_fma_f32 v[6:7], v[0:1], v[6:7], v[10:11] op_sel_hi:[1,0,1]
	s_nop 0
	v_mov_b32_e32 v13, v7
	v_pk_add_f32 v[6:7], v[12:13], v[54:55]
	s_nop 0
	v_lshl_add_u64 v[4:5], v[4:5], 0, s[14:15]
	v_cvt_pk_bf16_f32 v14, v6, v177
	v_cvt_pk_bf16_f32 v15, v7, v177
	global_store_short v[4:5], v14, off offset:-1536
	global_store_short v[4:5], v15, off offset:-1408
	v_pk_mul_f32 v[10:11], v[2:3], v[6:7] op_sel:[0,1]
	s_nop 0
	v_pk_fma_f32 v[12:13], v[0:1], v[6:7], v[10:11] neg_lo:[0,0,1] neg_hi:[0,0,1]
	v_pk_fma_f32 v[6:7], v[0:1], v[6:7], v[10:11] op_sel_hi:[1,0,1]
	s_nop 0
	v_mov_b32_e32 v13, v7
	v_pk_add_f32 v[6:7], v[12:13], v[56:57]
	s_nop 0
	v_cvt_pk_bf16_f32 v14, v6, v177
	v_cvt_pk_bf16_f32 v15, v7, v177
	global_store_short v[4:5], v14, off offset:-768
	global_store_short v[4:5], v15, off offset:-640
	v_pk_mul_f32 v[10:11], v[2:3], v[6:7] op_sel:[0,1]
	s_nop 0
	v_pk_fma_f32 v[12:13], v[0:1], v[6:7], v[10:11] neg_lo:[0,0,1] neg_hi:[0,0,1]
	v_pk_fma_f32 v[6:7], v[0:1], v[6:7], v[10:11] op_sel_hi:[1,0,1]
	s_nop 0
	v_mov_b32_e32 v13, v7
	v_pk_add_f32 v[6:7], v[12:13], v[58:59]
	s_nop 0
	v_cvt_pk_bf16_f32 v14, v6, v177
	v_cvt_pk_bf16_f32 v15, v7, v177
	global_store_short v[4:5], v14, off
	global_store_short v[4:5], v15, off offset:128
	v_pk_mul_f32 v[10:11], v[2:3], v[6:7] op_sel:[0,1]
	s_nop 0
	v_pk_fma_f32 v[12:13], v[0:1], v[6:7], v[10:11] neg_lo:[0,0,1] neg_hi:[0,0,1]
	v_pk_fma_f32 v[6:7], v[0:1], v[6:7], v[10:11] op_sel_hi:[1,0,1]
	s_nop 0
	v_mov_b32_e32 v13, v7
	v_pk_add_f32 v[6:7], v[12:13], v[60:61]
	s_nop 0
	v_cvt_pk_bf16_f32 v14, v6, v177
	v_cvt_pk_bf16_f32 v15, v7, v177
	global_store_short v[4:5], v14, off offset:768
	global_store_short v[4:5], v15, off offset:896
	v_pk_mul_f32 v[10:11], v[2:3], v[6:7] op_sel:[0,1]
	s_nop 0
	v_pk_fma_f32 v[12:13], v[0:1], v[6:7], v[10:11] neg_lo:[0,0,1] neg_hi:[0,0,1]
	v_pk_fma_f32 v[6:7], v[0:1], v[6:7], v[10:11] op_sel_hi:[1,0,1]
	s_nop 0
	v_mov_b32_e32 v13, v7
	v_pk_add_f32 v[6:7], v[12:13], v[62:63]
	s_nop 0
	v_lshl_add_u64 v[4:5], v[4:5], 0, s[14:15]
	v_cvt_pk_bf16_f32 v14, v6, v177
	v_cvt_pk_bf16_f32 v15, v7, v177
	global_store_short v[4:5], v14, off offset:-1536
	global_store_short v[4:5], v15, off offset:-1408
	v_pk_mul_f32 v[10:11], v[2:3], v[6:7] op_sel:[0,1]
	s_nop 0
	v_pk_fma_f32 v[12:13], v[0:1], v[6:7], v[10:11] neg_lo:[0,0,1] neg_hi:[0,0,1]
	v_pk_fma_f32 v[6:7], v[0:1], v[6:7], v[10:11] op_sel_hi:[1,0,1]
	s_nop 0
	v_mov_b32_e32 v13, v7
	v_pk_add_f32 v[6:7], v[12:13], v[64:65]
	s_nop 0
	v_cvt_pk_bf16_f32 v14, v6, v177
	v_cvt_pk_bf16_f32 v15, v7, v177
	global_store_short v[4:5], v14, off offset:-768
	global_store_short v[4:5], v15, off offset:-640
	v_pk_mul_f32 v[10:11], v[2:3], v[6:7] op_sel:[0,1]
	s_nop 0
	v_pk_fma_f32 v[12:13], v[0:1], v[6:7], v[10:11] neg_lo:[0,0,1] neg_hi:[0,0,1]
	v_pk_fma_f32 v[6:7], v[0:1], v[6:7], v[10:11] op_sel_hi:[1,0,1]
	s_nop 0
	v_mov_b32_e32 v13, v7
	v_pk_add_f32 v[6:7], v[12:13], v[66:67]
	s_nop 0
	v_cvt_pk_bf16_f32 v14, v6, v177
	v_cvt_pk_bf16_f32 v15, v7, v177
	global_store_short v[4:5], v14, off
	global_store_short v[4:5], v15, off offset:128
	v_pk_mul_f32 v[10:11], v[2:3], v[6:7] op_sel:[0,1]
	s_nop 0
	v_pk_fma_f32 v[12:13], v[0:1], v[6:7], v[10:11] neg_lo:[0,0,1] neg_hi:[0,0,1]
	v_pk_fma_f32 v[6:7], v[0:1], v[6:7], v[10:11] op_sel_hi:[1,0,1]
	s_nop 0
	v_mov_b32_e32 v13, v7
	v_pk_add_f32 v[6:7], v[12:13], v[68:69]
	s_nop 0
	v_cvt_pk_bf16_f32 v14, v6, v177
	v_cvt_pk_bf16_f32 v15, v7, v177
	global_store_short v[4:5], v14, off offset:768
	global_store_short v[4:5], v15, off offset:896
	v_pk_mul_f32 v[10:11], v[2:3], v[6:7] op_sel:[0,1]
	s_nop 0
	v_pk_fma_f32 v[12:13], v[0:1], v[6:7], v[10:11] neg_lo:[0,0,1] neg_hi:[0,0,1]
	v_pk_fma_f32 v[6:7], v[0:1], v[6:7], v[10:11] op_sel_hi:[1,0,1]
	s_nop 0
	v_mov_b32_e32 v13, v7
	v_pk_add_f32 v[6:7], v[12:13], v[70:71]
	s_nop 0
	v_lshl_add_u64 v[4:5], v[4:5], 0, s[14:15]
	v_cvt_pk_bf16_f32 v14, v6, v177
	v_cvt_pk_bf16_f32 v15, v7, v177
	global_store_short v[4:5], v14, off offset:-1536
	global_store_short v[4:5], v15, off offset:-1408
	v_pk_mul_f32 v[10:11], v[2:3], v[6:7] op_sel:[0,1]
	s_nop 0
	v_pk_fma_f32 v[12:13], v[0:1], v[6:7], v[10:11] neg_lo:[0,0,1] neg_hi:[0,0,1]
	v_pk_fma_f32 v[6:7], v[0:1], v[6:7], v[10:11] op_sel_hi:[1,0,1]
	s_nop 0
	v_mov_b32_e32 v13, v7
	v_pk_add_f32 v[6:7], v[12:13], v[72:73]
	s_nop 0
	v_cvt_pk_bf16_f32 v14, v6, v177
	v_cvt_pk_bf16_f32 v15, v7, v177
	global_store_short v[4:5], v14, off offset:-768
	global_store_short v[4:5], v15, off offset:-640
	v_pk_mul_f32 v[10:11], v[2:3], v[6:7] op_sel:[0,1]
	s_nop 0
	v_pk_fma_f32 v[12:13], v[0:1], v[6:7], v[10:11] neg_lo:[0,0,1] neg_hi:[0,0,1]
	v_pk_fma_f32 v[6:7], v[0:1], v[6:7], v[10:11] op_sel_hi:[1,0,1]
	s_nop 0
	v_mov_b32_e32 v13, v7
	v_pk_add_f32 v[6:7], v[12:13], v[74:75]
	s_nop 0
	v_cvt_pk_bf16_f32 v14, v6, v177
	v_cvt_pk_bf16_f32 v15, v7, v177
	global_store_short v[4:5], v14, off
	global_store_short v[4:5], v15, off offset:128
	v_pk_mul_f32 v[10:11], v[2:3], v[6:7] op_sel:[0,1]
	s_nop 0
	v_pk_fma_f32 v[12:13], v[0:1], v[6:7], v[10:11] neg_lo:[0,0,1] neg_hi:[0,0,1]
	v_pk_fma_f32 v[6:7], v[0:1], v[6:7], v[10:11] op_sel_hi:[1,0,1]
	s_nop 0
	v_mov_b32_e32 v13, v7
	v_pk_add_f32 v[6:7], v[12:13], v[76:77]
	s_nop 0
	v_cvt_pk_bf16_f32 v14, v6, v177
	v_cvt_pk_bf16_f32 v15, v7, v177
	global_store_short v[4:5], v14, off offset:768
	global_store_short v[4:5], v15, off offset:896
	v_pk_mul_f32 v[10:11], v[2:3], v[6:7] op_sel:[0,1]
	s_nop 0
	v_pk_fma_f32 v[12:13], v[0:1], v[6:7], v[10:11] neg_lo:[0,0,1] neg_hi:[0,0,1]
	v_pk_fma_f32 v[6:7], v[0:1], v[6:7], v[10:11] op_sel_hi:[1,0,1]
	s_nop 0
	v_mov_b32_e32 v13, v7
	v_pk_add_f32 v[6:7], v[12:13], v[78:79]
	s_nop 0
	v_lshl_add_u64 v[4:5], v[4:5], 0, s[14:15]
	s_cmp_eq_u32 s28, 0x10000
	s_cbranch_scc0 .LBB0_1632
	s_mov_b32 s5, s33
	s_waitcnt vmcnt(0)
	s_barrier
	s_mov_b32 s10, s73
	v_lshl_or_b32 v9, s5, 6, v195
	s_mov_b32 s10, 0x1ffffe0
	v_ashrrev_i32_e32 v1, 31, v9
	v_lshrrev_b32_e32 v1, 26, v1
	v_add_u32_e32 v1, v9, v1
	v_ashrrev_i32_e32 v8, 6, v1
	v_bfe_i32 v1, v9, 27, 1
	v_lshlrev_b32_e32 v0, 4, v9
	v_lshrrev_b32_e32 v1, 22, v1
	v_add_u32_e32 v1, v0, v1
	v_and_b32_e32 v1, 0xfffffc00, v1
	v_sub_u32_e32 v1, v0, v1
	v_lshrrev_b32_e32 v2, 4, v1
	v_bitop3_b32 v1, v2, v1, 32 bitop3:0x6c
	v_ashrrev_i32_e32 v3, 31, v1
	v_lshrrev_b32_e32 v3, 26, v3
	v_lshlrev_b32_e32 v2, 3, v8
	v_add_u32_e32 v3, v1, v3
	v_and_b32_e32 v2, -16, v2
	v_ashrrev_i32_e32 v10, 6, v3
	v_and_b32_e32 v3, 0xc0, v3
	v_add_u32_e32 v2, v10, v2
	v_lshlrev_b32_e32 v4, 5, v8
	v_sub_u32_e32 v1, v1, v3
	v_and_b32_e32 v11, 32, v4
	v_ashrrev_i16_sdwa v1, v193, sext(v1) dst_sel:DWORD dst_unused:UNUSED_PAD src0_sel:DWORD src1_sel:BYTE_0
	v_lshlrev_b32_e32 v3, 1, v2
	v_lshrrev_b32_e32 v4, 2, v2
	v_and_b32_e32 v5, 3, v10
	v_bfe_i32 v12, v1, 0, 16
	v_and_b32_e32 v3, 24, v3
	v_and_b32_e32 v4, 4, v4
	v_and_or_b32 v5, v2, s10, v5
	s_movk_i32 s5, 0x180
	v_add_u32_e32 v1, v11, v12
	v_or3_b32 v3, v5, v4, v3
	v_mul_lo_u32 v2, v2, s5
	v_add_lshl_u32 v136, v1, v2, 1
	v_mul_lo_u32 v2, v3, s5
	v_add_u32_e32 v0, 0x2000, v0
	v_add_lshl_u32 v138, v2, v1, 1
	v_ashrrev_i32_e32 v1, 31, v0
	v_lshrrev_b32_e32 v1, 22, v1
	v_add_u32_e32 v1, v0, v1
	v_ashrrev_i32_e32 v13, 10, v1
	v_mul_i32_i24_e32 v1, 0x400, v13
	v_sub_u32_e32 v0, v0, v1
	v_lshrrev_b32_e32 v1, 4, v0
	v_bitop3_b32 v0, v1, v0, 32 bitop3:0x6c
	v_ashrrev_i32_e32 v2, 31, v0
	v_lshrrev_b32_e32 v2, 26, v2
	v_lshlrev_b32_e32 v1, 3, v13
	v_add_u32_e32 v2, v0, v2
	v_and_b32_e32 v1, -16, v1
	v_ashrrev_i32_e32 v14, 6, v2
	v_and_b32_e32 v2, 0xc0, v2
	v_add_u32_e32 v1, v14, v1
	v_lshlrev_b32_e32 v3, 5, v13
	v_sub_u32_e32 v0, v0, v2
	v_readfirstlane_b32 s15, v9
	v_and_b32_e32 v15, 32, v3
	v_ashrrev_i16_sdwa v0, v193, sext(v0) dst_sel:DWORD dst_unused:UNUSED_PAD src0_sel:DWORD src1_sel:BYTE_0
	v_lshlrev_b32_e32 v2, 1, v1
	v_lshrrev_b32_e32 v3, 2, v1
	v_and_b32_e32 v4, 3, v14
	v_bfe_i32 v16, v0, 0, 16
	v_and_b32_e32 v2, 24, v2
	v_and_b32_e32 v3, 4, v3
	v_and_or_b32 v4, v1, s10, v4
	s_ashr_i32 s34, s15, 6
	s_ashr_i32 s14, s15, 8
	v_add_u32_e32 v0, v15, v16
	v_or3_b32 v2, v4, v3, v2
	v_mul_lo_u32 v1, v1, s5
	s_lshl_b32 s25, s34, 10
	s_mul_i32 s10, s24, 0x30000
	v_add_lshl_u32 v140, v0, v1, 1
	v_mul_lo_u32 v1, v2, s5
	s_mul_hi_i32 s5, s24, 0x30000
	s_add_u32 s28, s83, s10
	s_addc_u32 s29, s84, s5
	s_add_i32 s52, s25, 0
	s_add_i32 m0, s52, 0x10000
	v_add_lshl_u32 v142, v1, v0, 1
	global_load_lds_dwordx4 v138, s[28:29]
	s_add_i32 m0, s52, 0x12000
	s_add_u32 s36, s28, 0x18000
	global_load_lds_dwordx4 v142, s[28:29]
	s_addc_u32 s37, s29, 0
	s_add_i32 m0, s52, 0x14000
	s_add_i32 s53, s52, 0x2000
	global_load_lds_dwordx4 v138, s[36:37]
	s_add_i32 m0, s52, 0x16000
	s_add_i32 s54, s52, 0x4000
	global_load_lds_dwordx4 v142, s[36:37]
	s_mov_b32 m0, s52
	s_add_i32 s55, s52, 0x6000
	global_load_lds_dwordx4 v136, s[26:27]
	s_mov_b32 m0, s53
	v_mov_b32_e32 v139, v177
	global_load_lds_dwordx4 v140, s[26:27]
	s_mov_b32 m0, s54
	v_mov_b32_e32 v143, v177
	global_load_lds_dwordx4 v136, s[30:31]
	s_mov_b32 m0, s55
	v_mov_b32_e32 v137, v177
	global_load_lds_dwordx4 v140, s[30:31]
	v_mov_b32_e32 v141, v177
	s_cmp_eq_u32 s14, 1
	v_lshl_add_u64 v[6:7], s[28:29], 0, v[138:139]
	v_lshl_add_u64 v[4:5], s[28:29], 0, v[142:143]
	v_lshl_add_u64 v[0:1], s[26:27], 0, v[136:137]
	s_cselect_b64 s[30:31], -1, 0
	s_cmp_lg_u32 s14, 1
	v_lshl_add_u64 v[2:3], s[26:27], 0, v[140:141]
	s_cbranch_scc1 .LBB0_1635
	s_barrier
